# barrier-hosted expert weight conversion (14 slots x 7 barriers) + x->fp8 prologue loop software-pipelined with two register sets
# speedup vs baseline: 1.0052x; 1.0000x over previous
.LBB0_50:
	s_ashr_i32 s97, s96, 31
	s_lshl_b64 s[0:1], s[96:97], 9
	v_ashrrev_i32_e32 v3, 31, v2
	v_lshl_add_u64 v[4:5], s[0:1], 0, v[2:3]
	s_mov_b64 s[0:1], 0x400000
	v_cmp_gt_u64_e32 vcc, s[0:1], v[4:5]
	s_and_saveexec_b64 s[0:1], vcc
	s_cbranch_execz .LBB0_53
	s_ashr_i32 s75, s74, 31
	s_lshl_b64 s[6:7], s[74:75], 9
	s_lshl_b64 s[2:3], s[96:97], 13
	s_add_u32 s2, s62, s2
	s_addc_u32 s3, s63, s3
	v_lshl_add_u64 v[6:7], v[2:3], 4, s[2:3]
	s_mov_b64 s[2:3], 0xe000000
	v_lshl_add_u64 v[6:7], v[6:7], 0, s[2:3]
	s_lshl_b64 s[8:9], s[74:75], 13
	s_lshl_b64 s[2:3], s[96:97], 15
	s_add_u32 s2, s80, s2
	v_lshlrev_b64 v[2:3], 6, v[2:3]
	s_addc_u32 s3, s81, s3
	v_lshl_add_u64 v[2:3], s[2:3], 0, v[2:3]
	v_lshl_add_u64 v[2:3], v[2:3], 0, 32
	s_lshl_b64 s[10:11], s[74:75], 15
	s_mov_b64 s[12:13], 0
	s_mov_b64 s[14:15], 0x3fffff
	s_cmp_lg_u32 s74, 0x100
	s_cbranch_scc1 .LBB0_52
	s_mov_b32 s16, 15
	global_load_dwordx4 v[8:11], v[2:3], off offset:-32 nt
	global_load_dwordx4 v[12:15], v[2:3], off offset:-16 nt
	global_load_dwordx4 v[16:19], v[2:3], off nt
	global_load_dwordx4 v[20:23], v[2:3], off offset:16 nt
	v_lshl_add_u64 v[2:3], v[2:3], 0, s[10:11]
	global_load_dwordx4 v[28:31], v[2:3], off offset:-32 nt
	global_load_dwordx4 v[32:35], v[2:3], off offset:-16 nt
	global_load_dwordx4 v[36:39], v[2:3], off nt
	global_load_dwordx4 v[40:43], v[2:3], off offset:16 nt
	v_lshl_add_u64 v[2:3], v[2:3], 0, s[10:11]
	s_waitcnt vmcnt(4)
	v_cvt_pk_fp8_f32 v24, v8, v9
	v_cvt_pk_fp8_f32 v25, v12, v13
	v_cvt_pk_fp8_f32 v26, v16, v17
	v_cvt_pk_fp8_f32 v27, v20, v21
	v_cvt_pk_fp8_f32 v24, v10, v11 op_sel:[0,0,1]
	v_cvt_pk_fp8_f32 v25, v14, v15 op_sel:[0,0,1]
	v_cvt_pk_fp8_f32 v26, v18, v19 op_sel:[0,0,1]
	v_cvt_pk_fp8_f32 v27, v22, v23 op_sel:[0,0,1]
	global_store_dwordx4 v[6:7], v[24:27], off
	v_lshl_add_u64 v[6:7], v[6:7], 0, s[8:9]
.Lx_loop:
	global_load_dwordx4 v[8:11], v[2:3], off offset:-32 nt
	global_load_dwordx4 v[12:15], v[2:3], off offset:-16 nt
	global_load_dwordx4 v[16:19], v[2:3], off nt
	global_load_dwordx4 v[20:23], v[2:3], off offset:16 nt
	v_lshl_add_u64 v[2:3], v[2:3], 0, s[10:11]
	s_waitcnt vmcnt(5)
	v_cvt_pk_fp8_f32 v44, v28, v29
	v_cvt_pk_fp8_f32 v45, v32, v33
	v_cvt_pk_fp8_f32 v46, v36, v37
	v_cvt_pk_fp8_f32 v47, v40, v41
	v_cvt_pk_fp8_f32 v44, v30, v31 op_sel:[0,0,1]
	v_cvt_pk_fp8_f32 v45, v34, v35 op_sel:[0,0,1]
	v_cvt_pk_fp8_f32 v46, v38, v39 op_sel:[0,0,1]
	v_cvt_pk_fp8_f32 v47, v42, v43 op_sel:[0,0,1]
	global_store_dwordx4 v[6:7], v[44:47], off
	v_lshl_add_u64 v[6:7], v[6:7], 0, s[8:9]
	global_load_dwordx4 v[28:31], v[2:3], off offset:-32 nt
	global_load_dwordx4 v[32:35], v[2:3], off offset:-16 nt
	global_load_dwordx4 v[36:39], v[2:3], off nt
	global_load_dwordx4 v[40:43], v[2:3], off offset:16 nt
	v_lshl_add_u64 v[2:3], v[2:3], 0, s[10:11]
	s_waitcnt vmcnt(5)
	v_cvt_pk_fp8_f32 v24, v8, v9
	v_cvt_pk_fp8_f32 v25, v12, v13
	v_cvt_pk_fp8_f32 v26, v16, v17
	v_cvt_pk_fp8_f32 v27, v20, v21
	v_cvt_pk_fp8_f32 v24, v10, v11 op_sel:[0,0,1]
	v_cvt_pk_fp8_f32 v25, v14, v15 op_sel:[0,0,1]
	v_cvt_pk_fp8_f32 v26, v18, v19 op_sel:[0,0,1]
	v_cvt_pk_fp8_f32 v27, v22, v23 op_sel:[0,0,1]
	global_store_dwordx4 v[6:7], v[24:27], off
	v_lshl_add_u64 v[6:7], v[6:7], 0, s[8:9]
	s_sub_i32 s16, s16, 1
	s_cmp_lg_u32 s16, 0
	s_cbranch_scc1 .Lx_loop
	s_waitcnt vmcnt(1)
	v_cvt_pk_fp8_f32 v44, v28, v29
	v_cvt_pk_fp8_f32 v45, v32, v33
	v_cvt_pk_fp8_f32 v46, v36, v37
	v_cvt_pk_fp8_f32 v47, v40, v41
	v_cvt_pk_fp8_f32 v44, v30, v31 op_sel:[0,0,1]
	v_cvt_pk_fp8_f32 v45, v34, v35 op_sel:[0,0,1]
	v_cvt_pk_fp8_f32 v46, v38, v39 op_sel:[0,0,1]
	v_cvt_pk_fp8_f32 v47, v42, v43 op_sel:[0,0,1]
	global_store_dwordx4 v[6:7], v[44:47], off
	v_lshl_add_u64 v[6:7], v[6:7], 0, s[8:9]
	s_branch .LBB0_53

.Lhw_seam0:
	s_mov_b64 exec, -1
	v_readlane_b32 s2, v239, 0
	s_lshr_b32 s2, s2, 6
	s_add_i32 s2, s2, -1
	s_cmp_gt_u32 s2, 13
	s_cbranch_scc1 .Lhw_seam0_done
	s_add_i32 s2, s2, 0
	s_mul_i32 s2, s2, s74
	v_readlane_b32 s9, v239, 23
	s_lshr_b32 s9, s9, 3
	s_add_i32 s2, s2, s9
	s_cmp_gt_u32 s2, 24575
	s_cbranch_scc1 .Lhw_seam0_done
	v_mbcnt_lo_u32_b32 v178, -1, 0
	v_mbcnt_hi_u32_b32 v178, -1, v178
	v_and_b32_e32 v179, 60, v178
	v_lshlrev_b32_e32 v179, 10, v179
	v_and_b32_e32 v180, 3, v178
	v_lshl_or_b32 v179, v180, 4, v179
	v_add_u32_e32 v180, 0x400, v179
	v_add_u32_e32 v181, 0x800, v179
	v_add_u32_e32 v190, 0xc00, v179
	v_lshlrev_b32_e32 v178, 2, v178
	s_cmp_lt_u32 s2, 16384
	s_cbranch_scc0 .Lhw_dn_s0_0
	s_lshr_b32 s9, s2, 9
	s_bfe_u32 s32, s2, 0x40005
	s_and_b32 s53, s2, 31
	s_lshl_b32 s69, s9, 23
	s_lshl_b32 s100, s32, 19
	s_add_i32 s69, s69, s100
	s_lshl_b32 s100, s53, 8
	s_add_i32 s69, s69, s100
	s_lshl_b32 s98, s9, 11
	s_bfe_u32 s100, s53, 0x30001
	s_lshl_b32 s100, s100, 8
	s_add_i32 s98, s98, s100
	s_lshr_b32 s100, s53, 4
	s_lshl_b32 s100, s100, 7
	s_add_i32 s98, s98, s100
	s_and_b32 s100, s53, 1
	s_lshl_b32 s100, s100, 6
	s_add_i32 s98, s98, s100
	s_lshl_b32 s98, s98, 10
	s_lshl_b32 s100, s32, 6
	s_add_i32 s98, s98, s100
	s_add_i32 s98, s98, 0x2000000
	v_readlane_b32 s82, v239, 11
	v_readlane_b32 s83, v239, 12
	s_movk_i32 s89, 8192
	s_branch .Lhw_go_s0_0

.Lhw_go_s0_0:
	s_add_u32 s100, s82, s69
	s_addc_u32 s101, s83, 0
	v_readlane_b32 s82, v239, 44
	v_readlane_b32 s83, v239, 45
	s_add_u32 s82, s82, s98
	s_addc_u32 s83, s83, 0
	global_load_dword v34, v178, s[100:101] nt
	s_add_u32 s100, s100, s89
	s_addc_u32 s101, s101, 0
	global_load_dword v35, v178, s[100:101] nt
	s_add_u32 s100, s100, s89
	s_addc_u32 s101, s101, 0
	global_load_dword v36, v178, s[100:101] nt
	s_add_u32 s100, s100, s89
	s_addc_u32 s101, s101, 0
	global_load_dword v37, v178, s[100:101] nt
	s_add_u32 s100, s100, s89
	s_addc_u32 s101, s101, 0
	global_load_dword v38, v178, s[100:101] nt
	s_add_u32 s100, s100, s89
	s_addc_u32 s101, s101, 0
	global_load_dword v39, v178, s[100:101] nt
	s_add_u32 s100, s100, s89
	s_addc_u32 s101, s101, 0
	global_load_dword v40, v178, s[100:101] nt
	s_add_u32 s100, s100, s89
	s_addc_u32 s101, s101, 0
	global_load_dword v41, v178, s[100:101] nt
	s_add_u32 s100, s100, s89
	s_addc_u32 s101, s101, 0
	global_load_dword v42, v178, s[100:101] nt
	s_add_u32 s100, s100, s89
	s_addc_u32 s101, s101, 0
	global_load_dword v43, v178, s[100:101] nt
	s_add_u32 s100, s100, s89
	s_addc_u32 s101, s101, 0
	global_load_dword v44, v178, s[100:101] nt
	s_add_u32 s100, s100, s89
	s_addc_u32 s101, s101, 0
	global_load_dword v45, v178, s[100:101] nt
	s_add_u32 s100, s100, s89
	s_addc_u32 s101, s101, 0
	global_load_dword v46, v178, s[100:101] nt
	s_add_u32 s100, s100, s89
	s_addc_u32 s101, s101, 0
	global_load_dword v47, v178, s[100:101] nt
	s_add_u32 s100, s100, s89
	s_addc_u32 s101, s101, 0
	global_load_dword v48, v178, s[100:101] nt
	s_add_u32 s100, s100, s89
	s_addc_u32 s101, s101, 0
	global_load_dword v49, v178, s[100:101] nt
	s_add_u32 s100, s100, s89
	s_addc_u32 s101, s101, 0
	global_load_dword v50, v178, s[100:101] nt
	s_add_u32 s100, s100, s89
	s_addc_u32 s101, s101, 0
	global_load_dword v51, v178, s[100:101] nt
	s_add_u32 s100, s100, s89
	s_addc_u32 s101, s101, 0
	global_load_dword v52, v178, s[100:101] nt
	s_add_u32 s100, s100, s89
	s_addc_u32 s101, s101, 0
	global_load_dword v53, v178, s[100:101] nt
	s_add_u32 s100, s100, s89
	s_addc_u32 s101, s101, 0
	global_load_dword v54, v178, s[100:101] nt
	s_add_u32 s100, s100, s89
	s_addc_u32 s101, s101, 0
	global_load_dword v55, v178, s[100:101] nt
	s_add_u32 s100, s100, s89
	s_addc_u32 s101, s101, 0
	global_load_dword v56, v178, s[100:101] nt
	s_add_u32 s100, s100, s89
	s_addc_u32 s101, s101, 0
	global_load_dword v57, v178, s[100:101] nt
	s_add_u32 s100, s100, s89
	s_addc_u32 s101, s101, 0
	global_load_dword v58, v178, s[100:101] nt
	s_add_u32 s100, s100, s89
	s_addc_u32 s101, s101, 0
	global_load_dword v59, v178, s[100:101] nt
	s_add_u32 s100, s100, s89
	s_addc_u32 s101, s101, 0
	global_load_dword v60, v178, s[100:101] nt
	s_add_u32 s100, s100, s89
	s_addc_u32 s101, s101, 0
	global_load_dword v61, v178, s[100:101] nt
	s_add_u32 s100, s100, s89
	s_addc_u32 s101, s101, 0
	global_load_dword v62, v178, s[100:101] nt
	s_add_u32 s100, s100, s89
	s_addc_u32 s101, s101, 0
	global_load_dword v63, v178, s[100:101] nt
	s_add_u32 s100, s100, s89
	s_addc_u32 s101, s101, 0
	global_load_dword v64, v178, s[100:101] nt
	s_add_u32 s100, s100, s89
	s_addc_u32 s101, s101, 0
	global_load_dword v65, v178, s[100:101] nt
	s_add_u32 s100, s100, s89
	s_addc_u32 s101, s101, 0
	global_load_dword v66, v178, s[100:101] nt
	s_add_u32 s100, s100, s89
	s_addc_u32 s101, s101, 0
	global_load_dword v67, v178, s[100:101] nt
	s_add_u32 s100, s100, s89
	s_addc_u32 s101, s101, 0
	global_load_dword v68, v178, s[100:101] nt
	s_add_u32 s100, s100, s89
	s_addc_u32 s101, s101, 0
	global_load_dword v69, v178, s[100:101] nt
	s_add_u32 s100, s100, s89
	s_addc_u32 s101, s101, 0
	global_load_dword v70, v178, s[100:101] nt
	s_add_u32 s100, s100, s89
	s_addc_u32 s101, s101, 0
	global_load_dword v71, v178, s[100:101] nt
	s_add_u32 s100, s100, s89
	s_addc_u32 s101, s101, 0
	global_load_dword v72, v178, s[100:101] nt
	s_add_u32 s100, s100, s89
	s_addc_u32 s101, s101, 0
	global_load_dword v73, v178, s[100:101] nt
	s_add_u32 s100, s100, s89
	s_addc_u32 s101, s101, 0
	global_load_dword v74, v178, s[100:101] nt
	s_add_u32 s100, s100, s89
	s_addc_u32 s101, s101, 0
	global_load_dword v75, v178, s[100:101] nt
	s_add_u32 s100, s100, s89
	s_addc_u32 s101, s101, 0
	global_load_dword v76, v178, s[100:101] nt
	s_add_u32 s100, s100, s89
	s_addc_u32 s101, s101, 0
	global_load_dword v77, v178, s[100:101] nt
	s_add_u32 s100, s100, s89
	s_addc_u32 s101, s101, 0
	global_load_dword v78, v178, s[100:101] nt
	s_add_u32 s100, s100, s89
	s_addc_u32 s101, s101, 0
	global_load_dword v79, v178, s[100:101] nt
	s_add_u32 s100, s100, s89
	s_addc_u32 s101, s101, 0
	global_load_dword v80, v178, s[100:101] nt
	s_add_u32 s100, s100, s89
	s_addc_u32 s101, s101, 0
	global_load_dword v81, v178, s[100:101] nt
	s_add_u32 s100, s100, s89
	s_addc_u32 s101, s101, 0
	global_load_dword v82, v178, s[100:101] nt
	s_add_u32 s100, s100, s89
	s_addc_u32 s101, s101, 0
	global_load_dword v83, v178, s[100:101] nt
	s_add_u32 s100, s100, s89
	s_addc_u32 s101, s101, 0
	global_load_dword v84, v178, s[100:101] nt
	s_add_u32 s100, s100, s89
	s_addc_u32 s101, s101, 0
	global_load_dword v85, v178, s[100:101] nt
	s_add_u32 s100, s100, s89
	s_addc_u32 s101, s101, 0
	global_load_dword v86, v178, s[100:101] nt
	s_add_u32 s100, s100, s89
	s_addc_u32 s101, s101, 0
	global_load_dword v87, v178, s[100:101] nt
	s_add_u32 s100, s100, s89
	s_addc_u32 s101, s101, 0
	global_load_dword v88, v178, s[100:101] nt
	s_add_u32 s100, s100, s89
	s_addc_u32 s101, s101, 0
	global_load_dword v89, v178, s[100:101] nt
	s_add_u32 s100, s100, s89
	s_addc_u32 s101, s101, 0
	global_load_dword v90, v178, s[100:101] nt
	s_add_u32 s100, s100, s89
	s_addc_u32 s101, s101, 0
	global_load_dword v91, v178, s[100:101] nt
	s_add_u32 s100, s100, s89
	s_addc_u32 s101, s101, 0
	global_load_dword v92, v178, s[100:101] nt
	s_add_u32 s100, s100, s89
	s_addc_u32 s101, s101, 0
	global_load_dword v93, v178, s[100:101] nt
	s_add_u32 s100, s100, s89
	s_addc_u32 s101, s101, 0
	global_load_dword v94, v178, s[100:101] nt
	s_add_u32 s100, s100, s89
	s_addc_u32 s101, s101, 0
	global_load_dword v95, v178, s[100:101] nt
	s_add_u32 s100, s100, s89
	s_addc_u32 s101, s101, 0
	global_load_dword v96, v178, s[100:101] nt
	s_add_u32 s100, s100, s89
	s_addc_u32 s101, s101, 0
	global_load_dword v97, v178, s[100:101] nt
	s_add_u32 s100, s100, s89
	s_addc_u32 s101, s101, 0
	s_waitcnt vmcnt(48)
	v_mul_f32_e32 v34, 0x42000000, v34
	v_mul_f32_e32 v35, 0x42000000, v35
	v_mul_f32_e32 v36, 0x42000000, v36
	v_mul_f32_e32 v37, 0x42000000, v37
	v_mul_f32_e32 v38, 0x42000000, v38
	v_mul_f32_e32 v39, 0x42000000, v39
	v_mul_f32_e32 v40, 0x42000000, v40
	v_mul_f32_e32 v41, 0x42000000, v41
	v_mul_f32_e32 v42, 0x42000000, v42
	v_mul_f32_e32 v43, 0x42000000, v43
	v_mul_f32_e32 v44, 0x42000000, v44
	v_mul_f32_e32 v45, 0x42000000, v45
	v_mul_f32_e32 v46, 0x42000000, v46
	v_mul_f32_e32 v47, 0x42000000, v47
	v_mul_f32_e32 v48, 0x42000000, v48
	v_mul_f32_e32 v49, 0x42000000, v49
	v_cvt_pk_fp8_f32 v154, v34, v35
	v_cvt_pk_fp8_f32 v155, v38, v39
	v_cvt_pk_fp8_f32 v156, v42, v43
	v_cvt_pk_fp8_f32 v157, v46, v47
	v_cvt_pk_fp8_f32 v154, v36, v37 op_sel:[0,0,1]
	v_cvt_pk_fp8_f32 v155, v40, v41 op_sel:[0,0,1]
	v_cvt_pk_fp8_f32 v156, v44, v45 op_sel:[0,0,1]
	v_cvt_pk_fp8_f32 v157, v48, v49 op_sel:[0,0,1]
	s_waitcnt vmcnt(32)
	v_mul_f32_e32 v50, 0x42000000, v50
	v_mul_f32_e32 v51, 0x42000000, v51
	v_mul_f32_e32 v52, 0x42000000, v52
	v_mul_f32_e32 v53, 0x42000000, v53
	v_mul_f32_e32 v54, 0x42000000, v54
	v_mul_f32_e32 v55, 0x42000000, v55
	v_mul_f32_e32 v56, 0x42000000, v56
	v_mul_f32_e32 v57, 0x42000000, v57
	v_mul_f32_e32 v58, 0x42000000, v58
	v_mul_f32_e32 v59, 0x42000000, v59
	v_mul_f32_e32 v60, 0x42000000, v60
	v_mul_f32_e32 v61, 0x42000000, v61
	v_mul_f32_e32 v62, 0x42000000, v62
	v_mul_f32_e32 v63, 0x42000000, v63
	v_mul_f32_e32 v64, 0x42000000, v64
	v_mul_f32_e32 v65, 0x42000000, v65
	v_cvt_pk_fp8_f32 v158, v50, v51
	v_cvt_pk_fp8_f32 v159, v54, v55
	v_cvt_pk_fp8_f32 v160, v58, v59
	v_cvt_pk_fp8_f32 v161, v62, v63
	v_cvt_pk_fp8_f32 v158, v52, v53 op_sel:[0,0,1]
	v_cvt_pk_fp8_f32 v159, v56, v57 op_sel:[0,0,1]
	v_cvt_pk_fp8_f32 v160, v60, v61 op_sel:[0,0,1]
	v_cvt_pk_fp8_f32 v161, v64, v65 op_sel:[0,0,1]
	s_waitcnt vmcnt(16)
	v_mul_f32_e32 v66, 0x42000000, v66
	v_mul_f32_e32 v67, 0x42000000, v67
	v_mul_f32_e32 v68, 0x42000000, v68
	v_mul_f32_e32 v69, 0x42000000, v69
	v_mul_f32_e32 v70, 0x42000000, v70
	v_mul_f32_e32 v71, 0x42000000, v71
	v_mul_f32_e32 v72, 0x42000000, v72
	v_mul_f32_e32 v73, 0x42000000, v73
	v_mul_f32_e32 v74, 0x42000000, v74
	v_mul_f32_e32 v75, 0x42000000, v75
	v_mul_f32_e32 v76, 0x42000000, v76
	v_mul_f32_e32 v77, 0x42000000, v77
	v_mul_f32_e32 v78, 0x42000000, v78
	v_mul_f32_e32 v79, 0x42000000, v79
	v_mul_f32_e32 v80, 0x42000000, v80
	v_mul_f32_e32 v81, 0x42000000, v81
	v_cvt_pk_fp8_f32 v162, v66, v67
	v_cvt_pk_fp8_f32 v163, v70, v71
	v_cvt_pk_fp8_f32 v164, v74, v75
	v_cvt_pk_fp8_f32 v165, v78, v79
	v_cvt_pk_fp8_f32 v162, v68, v69 op_sel:[0,0,1]
	v_cvt_pk_fp8_f32 v163, v72, v73 op_sel:[0,0,1]
	v_cvt_pk_fp8_f32 v164, v76, v77 op_sel:[0,0,1]
	v_cvt_pk_fp8_f32 v165, v80, v81 op_sel:[0,0,1]
	s_waitcnt vmcnt(0)
	v_mul_f32_e32 v82, 0x42000000, v82
	v_mul_f32_e32 v83, 0x42000000, v83
	v_mul_f32_e32 v84, 0x42000000, v84
	v_mul_f32_e32 v85, 0x42000000, v85
	v_mul_f32_e32 v86, 0x42000000, v86
	v_mul_f32_e32 v87, 0x42000000, v87
	v_mul_f32_e32 v88, 0x42000000, v88
	v_mul_f32_e32 v89, 0x42000000, v89
	v_mul_f32_e32 v90, 0x42000000, v90
	v_mul_f32_e32 v91, 0x42000000, v91
	v_mul_f32_e32 v92, 0x42000000, v92
	v_mul_f32_e32 v93, 0x42000000, v93
	v_mul_f32_e32 v94, 0x42000000, v94
	v_mul_f32_e32 v95, 0x42000000, v95
	v_mul_f32_e32 v96, 0x42000000, v96
	v_mul_f32_e32 v97, 0x42000000, v97
	v_cvt_pk_fp8_f32 v166, v82, v83
	v_cvt_pk_fp8_f32 v167, v86, v87
	v_cvt_pk_fp8_f32 v168, v90, v91
	v_cvt_pk_fp8_f32 v169, v94, v95
	v_cvt_pk_fp8_f32 v166, v84, v85 op_sel:[0,0,1]
	v_cvt_pk_fp8_f32 v167, v88, v89 op_sel:[0,0,1]
	v_cvt_pk_fp8_f32 v168, v92, v93 op_sel:[0,0,1]
	v_cvt_pk_fp8_f32 v169, v96, v97 op_sel:[0,0,1]
	s_mov_b32 vcc_lo, 0xaaaaaaaa
	s_mov_b32 vcc_hi, 0xaaaaaaaa
	s_nop 1
	v_cndmask_b32_dpp v170, v154, v158, vcc quad_perm:[1,0,3,2] row_mask:0xf bank_mask:0xf
	v_cndmask_b32_dpp v174, v162, v166, vcc quad_perm:[1,0,3,2] row_mask:0xf bank_mask:0xf
	v_cndmask_b32_dpp v171, v155, v159, vcc quad_perm:[1,0,3,2] row_mask:0xf bank_mask:0xf
	v_cndmask_b32_dpp v175, v163, v167, vcc quad_perm:[1,0,3,2] row_mask:0xf bank_mask:0xf
	v_cndmask_b32_dpp v172, v156, v160, vcc quad_perm:[1,0,3,2] row_mask:0xf bank_mask:0xf
	v_cndmask_b32_dpp v176, v164, v168, vcc quad_perm:[1,0,3,2] row_mask:0xf bank_mask:0xf
	v_cndmask_b32_dpp v173, v157, v161, vcc quad_perm:[1,0,3,2] row_mask:0xf bank_mask:0xf
	v_cndmask_b32_dpp v177, v165, v169, vcc quad_perm:[1,0,3,2] row_mask:0xf bank_mask:0xf
	s_mov_b32 vcc_lo, 0x55555555
	s_mov_b32 vcc_hi, 0x55555555
	s_nop 1
	v_cndmask_b32_dpp v154, v158, v154, vcc quad_perm:[1,0,3,2] row_mask:0xf bank_mask:0xf
	v_cndmask_b32_dpp v162, v166, v162, vcc quad_perm:[1,0,3,2] row_mask:0xf bank_mask:0xf
	v_cndmask_b32_dpp v155, v159, v155, vcc quad_perm:[1,0,3,2] row_mask:0xf bank_mask:0xf
	v_cndmask_b32_dpp v163, v167, v163, vcc quad_perm:[1,0,3,2] row_mask:0xf bank_mask:0xf
	v_cndmask_b32_dpp v156, v160, v156, vcc quad_perm:[1,0,3,2] row_mask:0xf bank_mask:0xf
	v_cndmask_b32_dpp v164, v168, v164, vcc quad_perm:[1,0,3,2] row_mask:0xf bank_mask:0xf
	v_cndmask_b32_dpp v157, v161, v157, vcc quad_perm:[1,0,3,2] row_mask:0xf bank_mask:0xf
	v_cndmask_b32_dpp v165, v169, v165, vcc quad_perm:[1,0,3,2] row_mask:0xf bank_mask:0xf
	s_mov_b32 vcc_lo, 0xcccccccc
	s_mov_b32 vcc_hi, 0xcccccccc
	s_nop 1
	v_cndmask_b32_dpp v158, v154, v162, vcc quad_perm:[2,3,0,1] row_mask:0xf bank_mask:0xf
	v_cndmask_b32_dpp v166, v170, v174, vcc quad_perm:[2,3,0,1] row_mask:0xf bank_mask:0xf
	v_cndmask_b32_dpp v159, v155, v163, vcc quad_perm:[2,3,0,1] row_mask:0xf bank_mask:0xf
	v_cndmask_b32_dpp v167, v171, v175, vcc quad_perm:[2,3,0,1] row_mask:0xf bank_mask:0xf
	v_cndmask_b32_dpp v160, v156, v164, vcc quad_perm:[2,3,0,1] row_mask:0xf bank_mask:0xf
	v_cndmask_b32_dpp v168, v172, v176, vcc quad_perm:[2,3,0,1] row_mask:0xf bank_mask:0xf
	v_cndmask_b32_dpp v161, v157, v165, vcc quad_perm:[2,3,0,1] row_mask:0xf bank_mask:0xf
	v_cndmask_b32_dpp v169, v173, v177, vcc quad_perm:[2,3,0,1] row_mask:0xf bank_mask:0xf
	s_mov_b32 vcc_lo, 0x33333333
	s_mov_b32 vcc_hi, 0x33333333
	s_nop 1
	v_cndmask_b32_dpp v154, v162, v154, vcc quad_perm:[2,3,0,1] row_mask:0xf bank_mask:0xf
	v_cndmask_b32_dpp v170, v174, v170, vcc quad_perm:[2,3,0,1] row_mask:0xf bank_mask:0xf
	v_cndmask_b32_dpp v155, v163, v155, vcc quad_perm:[2,3,0,1] row_mask:0xf bank_mask:0xf
	v_cndmask_b32_dpp v171, v175, v171, vcc quad_perm:[2,3,0,1] row_mask:0xf bank_mask:0xf
	v_cndmask_b32_dpp v156, v164, v156, vcc quad_perm:[2,3,0,1] row_mask:0xf bank_mask:0xf
	v_cndmask_b32_dpp v172, v176, v172, vcc quad_perm:[2,3,0,1] row_mask:0xf bank_mask:0xf
	v_cndmask_b32_dpp v157, v165, v157, vcc quad_perm:[2,3,0,1] row_mask:0xf bank_mask:0xf
	v_cndmask_b32_dpp v173, v177, v173, vcc quad_perm:[2,3,0,1] row_mask:0xf bank_mask:0xf
	global_store_dwordx4 v179, v[154:157], s[82:83] nt
	global_store_dwordx4 v180, v[170:173], s[82:83] nt
	global_store_dwordx4 v181, v[158:161], s[82:83] nt
	global_store_dwordx4 v190, v[166:169], s[82:83] nt
	v_readlane_b32 s2, v239, 0
	s_lshr_b32 s2, s2, 6
	s_add_i32 s2, s2, 6
	s_cmp_gt_u32 s2, 13
	s_cbranch_scc1 .Lhw_seam0_done
	s_add_i32 s2, s2, 0
	s_mul_i32 s2, s2, s74
	v_readlane_b32 s9, v239, 23
	s_lshr_b32 s9, s9, 3
	s_add_i32 s2, s2, s9
	s_cmp_gt_u32 s2, 24575
	s_cbranch_scc1 .Lhw_seam0_done
	v_mbcnt_lo_u32_b32 v178, -1, 0
	v_mbcnt_hi_u32_b32 v178, -1, v178
	v_and_b32_e32 v179, 60, v178
	v_lshlrev_b32_e32 v179, 10, v179
	v_and_b32_e32 v180, 3, v178
	v_lshl_or_b32 v179, v180, 4, v179
	v_add_u32_e32 v180, 0x400, v179
	v_add_u32_e32 v181, 0x800, v179
	v_add_u32_e32 v190, 0xc00, v179
	v_lshlrev_b32_e32 v178, 2, v178
	s_cmp_lt_u32 s2, 16384
	s_cbranch_scc0 .Lhw_dn_s0_1
	s_lshr_b32 s9, s2, 9
	s_bfe_u32 s32, s2, 0x40005
	s_and_b32 s53, s2, 31
	s_lshl_b32 s69, s9, 23
	s_lshl_b32 s100, s32, 19
	s_add_i32 s69, s69, s100
	s_lshl_b32 s100, s53, 8
	s_add_i32 s69, s69, s100
	s_lshl_b32 s98, s9, 11
	s_bfe_u32 s100, s53, 0x30001
	s_lshl_b32 s100, s100, 8
	s_add_i32 s98, s98, s100
	s_lshr_b32 s100, s53, 4
	s_lshl_b32 s100, s100, 7
	s_add_i32 s98, s98, s100
	s_and_b32 s100, s53, 1
	s_lshl_b32 s100, s100, 6
	s_add_i32 s98, s98, s100
	s_lshl_b32 s98, s98, 10
	s_lshl_b32 s100, s32, 6
	s_add_i32 s98, s98, s100
	s_add_i32 s98, s98, 0x2000000
	v_readlane_b32 s82, v239, 11
	v_readlane_b32 s83, v239, 12
	s_movk_i32 s89, 8192
	s_branch .Lhw_go_s0_1

.Lhw_seam1:
	s_mov_b64 exec, -1
	v_readlane_b32 s2, v239, 0
	s_lshr_b32 s2, s2, 6
	s_add_i32 s2, s2, -1
	s_cmp_gt_u32 s2, 13
	s_cbranch_scc1 .Lhw_seam1_done
	s_add_i32 s2, s2, 14
	s_mul_i32 s2, s2, s74
	v_readlane_b32 s9, v239, 23
	s_lshr_b32 s9, s9, 3
	s_add_i32 s2, s2, s9
	s_cmp_gt_u32 s2, 24575
	s_cbranch_scc1 .Lhw_seam1_done
	v_mbcnt_lo_u32_b32 v178, -1, 0
	v_mbcnt_hi_u32_b32 v178, -1, v178
	v_and_b32_e32 v179, 60, v178
	v_lshlrev_b32_e32 v179, 10, v179
	v_and_b32_e32 v180, 3, v178
	v_lshl_or_b32 v179, v180, 4, v179
	v_add_u32_e32 v180, 0x400, v179
	v_add_u32_e32 v181, 0x800, v179
	v_add_u32_e32 v190, 0xc00, v179
	v_lshlrev_b32_e32 v178, 2, v178
	s_cmp_lt_u32 s2, 16384
	s_cbranch_scc0 .Lhw_dn_s1_0
	s_lshr_b32 s9, s2, 9
	s_bfe_u32 s32, s2, 0x40005
	s_and_b32 s53, s2, 31
	s_lshl_b32 s69, s9, 23
	s_lshl_b32 s100, s32, 19
	s_add_i32 s69, s69, s100
	s_lshl_b32 s100, s53, 8
	s_add_i32 s69, s69, s100
	s_lshl_b32 s98, s9, 11
	s_bfe_u32 s100, s53, 0x30001
	s_lshl_b32 s100, s100, 8
	s_add_i32 s98, s98, s100
	s_lshr_b32 s100, s53, 4
	s_lshl_b32 s100, s100, 7
	s_add_i32 s98, s98, s100
	s_and_b32 s100, s53, 1
	s_lshl_b32 s100, s100, 6
	s_add_i32 s98, s98, s100
	s_lshl_b32 s98, s98, 10
	s_lshl_b32 s100, s32, 6
	s_add_i32 s98, s98, s100
	s_add_i32 s98, s98, 0x2000000
	v_readlane_b32 s82, v239, 11
	v_readlane_b32 s83, v239, 12
	s_movk_i32 s89, 8192
	s_branch .Lhw_go_s1_0

.Lhw_go_s1_0:
	s_add_u32 s100, s82, s69
	s_addc_u32 s101, s83, 0
	v_readlane_b32 s82, v239, 44
	v_readlane_b32 s83, v239, 45
	s_add_u32 s82, s82, s98
	s_addc_u32 s83, s83, 0
	global_load_dword v34, v178, s[100:101] nt
	s_add_u32 s100, s100, s89
	s_addc_u32 s101, s101, 0
	global_load_dword v35, v178, s[100:101] nt
	s_add_u32 s100, s100, s89
	s_addc_u32 s101, s101, 0
	global_load_dword v36, v178, s[100:101] nt
	s_add_u32 s100, s100, s89
	s_addc_u32 s101, s101, 0
	global_load_dword v37, v178, s[100:101] nt
	s_add_u32 s100, s100, s89
	s_addc_u32 s101, s101, 0
	global_load_dword v38, v178, s[100:101] nt
	s_add_u32 s100, s100, s89
	s_addc_u32 s101, s101, 0
	global_load_dword v39, v178, s[100:101] nt
	s_add_u32 s100, s100, s89
	s_addc_u32 s101, s101, 0
	global_load_dword v40, v178, s[100:101] nt
	s_add_u32 s100, s100, s89
	s_addc_u32 s101, s101, 0
	global_load_dword v41, v178, s[100:101] nt
	s_add_u32 s100, s100, s89
	s_addc_u32 s101, s101, 0
	global_load_dword v42, v178, s[100:101] nt
	s_add_u32 s100, s100, s89
	s_addc_u32 s101, s101, 0
	global_load_dword v43, v178, s[100:101] nt
	s_add_u32 s100, s100, s89
	s_addc_u32 s101, s101, 0
	global_load_dword v44, v178, s[100:101] nt
	s_add_u32 s100, s100, s89
	s_addc_u32 s101, s101, 0
	global_load_dword v45, v178, s[100:101] nt
	s_add_u32 s100, s100, s89
	s_addc_u32 s101, s101, 0
	global_load_dword v46, v178, s[100:101] nt
	s_add_u32 s100, s100, s89
	s_addc_u32 s101, s101, 0
	global_load_dword v47, v178, s[100:101] nt
	s_add_u32 s100, s100, s89
	s_addc_u32 s101, s101, 0
	global_load_dword v48, v178, s[100:101] nt
	s_add_u32 s100, s100, s89
	s_addc_u32 s101, s101, 0
	global_load_dword v49, v178, s[100:101] nt
	s_add_u32 s100, s100, s89
	s_addc_u32 s101, s101, 0
	global_load_dword v50, v178, s[100:101] nt
	s_add_u32 s100, s100, s89
	s_addc_u32 s101, s101, 0
	global_load_dword v51, v178, s[100:101] nt
	s_add_u32 s100, s100, s89
	s_addc_u32 s101, s101, 0
	global_load_dword v52, v178, s[100:101] nt
	s_add_u32 s100, s100, s89
	s_addc_u32 s101, s101, 0
	global_load_dword v53, v178, s[100:101] nt
	s_add_u32 s100, s100, s89
	s_addc_u32 s101, s101, 0
	global_load_dword v54, v178, s[100:101] nt
	s_add_u32 s100, s100, s89
	s_addc_u32 s101, s101, 0
	global_load_dword v55, v178, s[100:101] nt
	s_add_u32 s100, s100, s89
	s_addc_u32 s101, s101, 0
	global_load_dword v56, v178, s[100:101] nt
	s_add_u32 s100, s100, s89
	s_addc_u32 s101, s101, 0
	global_load_dword v57, v178, s[100:101] nt
	s_add_u32 s100, s100, s89
	s_addc_u32 s101, s101, 0
	global_load_dword v58, v178, s[100:101] nt
	s_add_u32 s100, s100, s89
	s_addc_u32 s101, s101, 0
	global_load_dword v59, v178, s[100:101] nt
	s_add_u32 s100, s100, s89
	s_addc_u32 s101, s101, 0
	global_load_dword v60, v178, s[100:101] nt
	s_add_u32 s100, s100, s89
	s_addc_u32 s101, s101, 0
	global_load_dword v61, v178, s[100:101] nt
	s_add_u32 s100, s100, s89
	s_addc_u32 s101, s101, 0
	global_load_dword v62, v178, s[100:101] nt
	s_add_u32 s100, s100, s89
	s_addc_u32 s101, s101, 0
	global_load_dword v63, v178, s[100:101] nt
	s_add_u32 s100, s100, s89
	s_addc_u32 s101, s101, 0
	global_load_dword v64, v178, s[100:101] nt
	s_add_u32 s100, s100, s89
	s_addc_u32 s101, s101, 0
	global_load_dword v65, v178, s[100:101] nt
	s_add_u32 s100, s100, s89
	s_addc_u32 s101, s101, 0
	global_load_dword v66, v178, s[100:101] nt
	s_add_u32 s100, s100, s89
	s_addc_u32 s101, s101, 0
	global_load_dword v67, v178, s[100:101] nt
	s_add_u32 s100, s100, s89
	s_addc_u32 s101, s101, 0
	global_load_dword v68, v178, s[100:101] nt
	s_add_u32 s100, s100, s89
	s_addc_u32 s101, s101, 0
	global_load_dword v69, v178, s[100:101] nt
	s_add_u32 s100, s100, s89
	s_addc_u32 s101, s101, 0
	global_load_dword v70, v178, s[100:101] nt
	s_add_u32 s100, s100, s89
	s_addc_u32 s101, s101, 0
	global_load_dword v71, v178, s[100:101] nt
	s_add_u32 s100, s100, s89
	s_addc_u32 s101, s101, 0
	global_load_dword v72, v178, s[100:101] nt
	s_add_u32 s100, s100, s89
	s_addc_u32 s101, s101, 0
	global_load_dword v73, v178, s[100:101] nt
	s_add_u32 s100, s100, s89
	s_addc_u32 s101, s101, 0
	global_load_dword v74, v178, s[100:101] nt
	s_add_u32 s100, s100, s89
	s_addc_u32 s101, s101, 0
	global_load_dword v75, v178, s[100:101] nt
	s_add_u32 s100, s100, s89
	s_addc_u32 s101, s101, 0
	global_load_dword v76, v178, s[100:101] nt
	s_add_u32 s100, s100, s89
	s_addc_u32 s101, s101, 0
	global_load_dword v77, v178, s[100:101] nt
	s_add_u32 s100, s100, s89
	s_addc_u32 s101, s101, 0
	global_load_dword v78, v178, s[100:101] nt
	s_add_u32 s100, s100, s89
	s_addc_u32 s101, s101, 0
	global_load_dword v79, v178, s[100:101] nt
	s_add_u32 s100, s100, s89
	s_addc_u32 s101, s101, 0
	global_load_dword v80, v178, s[100:101] nt
	s_add_u32 s100, s100, s89
	s_addc_u32 s101, s101, 0
	global_load_dword v81, v178, s[100:101] nt
	s_add_u32 s100, s100, s89
	s_addc_u32 s101, s101, 0
	global_load_dword v82, v178, s[100:101] nt
	s_add_u32 s100, s100, s89
	s_addc_u32 s101, s101, 0
	global_load_dword v83, v178, s[100:101] nt
	s_add_u32 s100, s100, s89
	s_addc_u32 s101, s101, 0
	global_load_dword v84, v178, s[100:101] nt
	s_add_u32 s100, s100, s89
	s_addc_u32 s101, s101, 0
	global_load_dword v85, v178, s[100:101] nt
	s_add_u32 s100, s100, s89
	s_addc_u32 s101, s101, 0
	global_load_dword v86, v178, s[100:101] nt
	s_add_u32 s100, s100, s89
	s_addc_u32 s101, s101, 0
	global_load_dword v87, v178, s[100:101] nt
	s_add_u32 s100, s100, s89
	s_addc_u32 s101, s101, 0
	global_load_dword v88, v178, s[100:101] nt
	s_add_u32 s100, s100, s89
	s_addc_u32 s101, s101, 0
	global_load_dword v89, v178, s[100:101] nt
	s_add_u32 s100, s100, s89
	s_addc_u32 s101, s101, 0
	global_load_dword v90, v178, s[100:101] nt
	s_add_u32 s100, s100, s89
	s_addc_u32 s101, s101, 0
	global_load_dword v91, v178, s[100:101] nt
	s_add_u32 s100, s100, s89
	s_addc_u32 s101, s101, 0
	global_load_dword v92, v178, s[100:101] nt
	s_add_u32 s100, s100, s89
	s_addc_u32 s101, s101, 0
	global_load_dword v93, v178, s[100:101] nt
	s_add_u32 s100, s100, s89
	s_addc_u32 s101, s101, 0
	global_load_dword v94, v178, s[100:101] nt
	s_add_u32 s100, s100, s89
	s_addc_u32 s101, s101, 0
	global_load_dword v95, v178, s[100:101] nt
	s_add_u32 s100, s100, s89
	s_addc_u32 s101, s101, 0
	global_load_dword v96, v178, s[100:101] nt
	s_add_u32 s100, s100, s89
	s_addc_u32 s101, s101, 0
	global_load_dword v97, v178, s[100:101] nt
	s_add_u32 s100, s100, s89
	s_addc_u32 s101, s101, 0
	s_waitcnt vmcnt(48)
	v_mul_f32_e32 v34, 0x42000000, v34
	v_mul_f32_e32 v35, 0x42000000, v35
	v_mul_f32_e32 v36, 0x42000000, v36
	v_mul_f32_e32 v37, 0x42000000, v37
	v_mul_f32_e32 v38, 0x42000000, v38
	v_mul_f32_e32 v39, 0x42000000, v39
	v_mul_f32_e32 v40, 0x42000000, v40
	v_mul_f32_e32 v41, 0x42000000, v41
	v_mul_f32_e32 v42, 0x42000000, v42
	v_mul_f32_e32 v43, 0x42000000, v43
	v_mul_f32_e32 v44, 0x42000000, v44
	v_mul_f32_e32 v45, 0x42000000, v45
	v_mul_f32_e32 v46, 0x42000000, v46
	v_mul_f32_e32 v47, 0x42000000, v47
	v_mul_f32_e32 v48, 0x42000000, v48
	v_mul_f32_e32 v49, 0x42000000, v49
	v_cvt_pk_fp8_f32 v154, v34, v35
	v_cvt_pk_fp8_f32 v155, v38, v39
	v_cvt_pk_fp8_f32 v156, v42, v43
	v_cvt_pk_fp8_f32 v157, v46, v47
	v_cvt_pk_fp8_f32 v154, v36, v37 op_sel:[0,0,1]
	v_cvt_pk_fp8_f32 v155, v40, v41 op_sel:[0,0,1]
	v_cvt_pk_fp8_f32 v156, v44, v45 op_sel:[0,0,1]
	v_cvt_pk_fp8_f32 v157, v48, v49 op_sel:[0,0,1]
	s_waitcnt vmcnt(32)
	v_mul_f32_e32 v50, 0x42000000, v50
	v_mul_f32_e32 v51, 0x42000000, v51
	v_mul_f32_e32 v52, 0x42000000, v52
	v_mul_f32_e32 v53, 0x42000000, v53
	v_mul_f32_e32 v54, 0x42000000, v54
	v_mul_f32_e32 v55, 0x42000000, v55
	v_mul_f32_e32 v56, 0x42000000, v56
	v_mul_f32_e32 v57, 0x42000000, v57
	v_mul_f32_e32 v58, 0x42000000, v58
	v_mul_f32_e32 v59, 0x42000000, v59
	v_mul_f32_e32 v60, 0x42000000, v60
	v_mul_f32_e32 v61, 0x42000000, v61
	v_mul_f32_e32 v62, 0x42000000, v62
	v_mul_f32_e32 v63, 0x42000000, v63
	v_mul_f32_e32 v64, 0x42000000, v64
	v_mul_f32_e32 v65, 0x42000000, v65
	v_cvt_pk_fp8_f32 v158, v50, v51
	v_cvt_pk_fp8_f32 v159, v54, v55
	v_cvt_pk_fp8_f32 v160, v58, v59
	v_cvt_pk_fp8_f32 v161, v62, v63
	v_cvt_pk_fp8_f32 v158, v52, v53 op_sel:[0,0,1]
	v_cvt_pk_fp8_f32 v159, v56, v57 op_sel:[0,0,1]
	v_cvt_pk_fp8_f32 v160, v60, v61 op_sel:[0,0,1]
	v_cvt_pk_fp8_f32 v161, v64, v65 op_sel:[0,0,1]
	s_waitcnt vmcnt(16)
	v_mul_f32_e32 v66, 0x42000000, v66
	v_mul_f32_e32 v67, 0x42000000, v67
	v_mul_f32_e32 v68, 0x42000000, v68
	v_mul_f32_e32 v69, 0x42000000, v69
	v_mul_f32_e32 v70, 0x42000000, v70
	v_mul_f32_e32 v71, 0x42000000, v71
	v_mul_f32_e32 v72, 0x42000000, v72
	v_mul_f32_e32 v73, 0x42000000, v73
	v_mul_f32_e32 v74, 0x42000000, v74
	v_mul_f32_e32 v75, 0x42000000, v75
	v_mul_f32_e32 v76, 0x42000000, v76
	v_mul_f32_e32 v77, 0x42000000, v77
	v_mul_f32_e32 v78, 0x42000000, v78
	v_mul_f32_e32 v79, 0x42000000, v79
	v_mul_f32_e32 v80, 0x42000000, v80
	v_mul_f32_e32 v81, 0x42000000, v81
	v_cvt_pk_fp8_f32 v162, v66, v67
	v_cvt_pk_fp8_f32 v163, v70, v71
	v_cvt_pk_fp8_f32 v164, v74, v75
	v_cvt_pk_fp8_f32 v165, v78, v79
	v_cvt_pk_fp8_f32 v162, v68, v69 op_sel:[0,0,1]
	v_cvt_pk_fp8_f32 v163, v72, v73 op_sel:[0,0,1]
	v_cvt_pk_fp8_f32 v164, v76, v77 op_sel:[0,0,1]
	v_cvt_pk_fp8_f32 v165, v80, v81 op_sel:[0,0,1]
	s_waitcnt vmcnt(0)
	v_mul_f32_e32 v82, 0x42000000, v82
	v_mul_f32_e32 v83, 0x42000000, v83
	v_mul_f32_e32 v84, 0x42000000, v84
	v_mul_f32_e32 v85, 0x42000000, v85
	v_mul_f32_e32 v86, 0x42000000, v86
	v_mul_f32_e32 v87, 0x42000000, v87
	v_mul_f32_e32 v88, 0x42000000, v88
	v_mul_f32_e32 v89, 0x42000000, v89
	v_mul_f32_e32 v90, 0x42000000, v90
	v_mul_f32_e32 v91, 0x42000000, v91
	v_mul_f32_e32 v92, 0x42000000, v92
	v_mul_f32_e32 v93, 0x42000000, v93
	v_mul_f32_e32 v94, 0x42000000, v94
	v_mul_f32_e32 v95, 0x42000000, v95
	v_mul_f32_e32 v96, 0x42000000, v96
	v_mul_f32_e32 v97, 0x42000000, v97
	v_cvt_pk_fp8_f32 v166, v82, v83
	v_cvt_pk_fp8_f32 v167, v86, v87
	v_cvt_pk_fp8_f32 v168, v90, v91
	v_cvt_pk_fp8_f32 v169, v94, v95
	v_cvt_pk_fp8_f32 v166, v84, v85 op_sel:[0,0,1]
	v_cvt_pk_fp8_f32 v167, v88, v89 op_sel:[0,0,1]
	v_cvt_pk_fp8_f32 v168, v92, v93 op_sel:[0,0,1]
	v_cvt_pk_fp8_f32 v169, v96, v97 op_sel:[0,0,1]
	s_mov_b32 vcc_lo, 0xaaaaaaaa
	s_mov_b32 vcc_hi, 0xaaaaaaaa
	s_nop 1
	v_cndmask_b32_dpp v170, v154, v158, vcc quad_perm:[1,0,3,2] row_mask:0xf bank_mask:0xf
	v_cndmask_b32_dpp v174, v162, v166, vcc quad_perm:[1,0,3,2] row_mask:0xf bank_mask:0xf
	v_cndmask_b32_dpp v171, v155, v159, vcc quad_perm:[1,0,3,2] row_mask:0xf bank_mask:0xf
	v_cndmask_b32_dpp v175, v163, v167, vcc quad_perm:[1,0,3,2] row_mask:0xf bank_mask:0xf
	v_cndmask_b32_dpp v172, v156, v160, vcc quad_perm:[1,0,3,2] row_mask:0xf bank_mask:0xf
	v_cndmask_b32_dpp v176, v164, v168, vcc quad_perm:[1,0,3,2] row_mask:0xf bank_mask:0xf
	v_cndmask_b32_dpp v173, v157, v161, vcc quad_perm:[1,0,3,2] row_mask:0xf bank_mask:0xf
	v_cndmask_b32_dpp v177, v165, v169, vcc quad_perm:[1,0,3,2] row_mask:0xf bank_mask:0xf
	s_mov_b32 vcc_lo, 0x55555555
	s_mov_b32 vcc_hi, 0x55555555
	s_nop 1
	v_cndmask_b32_dpp v154, v158, v154, vcc quad_perm:[1,0,3,2] row_mask:0xf bank_mask:0xf
	v_cndmask_b32_dpp v162, v166, v162, vcc quad_perm:[1,0,3,2] row_mask:0xf bank_mask:0xf
	v_cndmask_b32_dpp v155, v159, v155, vcc quad_perm:[1,0,3,2] row_mask:0xf bank_mask:0xf
	v_cndmask_b32_dpp v163, v167, v163, vcc quad_perm:[1,0,3,2] row_mask:0xf bank_mask:0xf
	v_cndmask_b32_dpp v156, v160, v156, vcc quad_perm:[1,0,3,2] row_mask:0xf bank_mask:0xf
	v_cndmask_b32_dpp v164, v168, v164, vcc quad_perm:[1,0,3,2] row_mask:0xf bank_mask:0xf
	v_cndmask_b32_dpp v157, v161, v157, vcc quad_perm:[1,0,3,2] row_mask:0xf bank_mask:0xf
	v_cndmask_b32_dpp v165, v169, v165, vcc quad_perm:[1,0,3,2] row_mask:0xf bank_mask:0xf
	s_mov_b32 vcc_lo, 0xcccccccc
	s_mov_b32 vcc_hi, 0xcccccccc
	s_nop 1
	v_cndmask_b32_dpp v158, v154, v162, vcc quad_perm:[2,3,0,1] row_mask:0xf bank_mask:0xf
	v_cndmask_b32_dpp v166, v170, v174, vcc quad_perm:[2,3,0,1] row_mask:0xf bank_mask:0xf
	v_cndmask_b32_dpp v159, v155, v163, vcc quad_perm:[2,3,0,1] row_mask:0xf bank_mask:0xf
	v_cndmask_b32_dpp v167, v171, v175, vcc quad_perm:[2,3,0,1] row_mask:0xf bank_mask:0xf
	v_cndmask_b32_dpp v160, v156, v164, vcc quad_perm:[2,3,0,1] row_mask:0xf bank_mask:0xf
	v_cndmask_b32_dpp v168, v172, v176, vcc quad_perm:[2,3,0,1] row_mask:0xf bank_mask:0xf
	v_cndmask_b32_dpp v161, v157, v165, vcc quad_perm:[2,3,0,1] row_mask:0xf bank_mask:0xf
	v_cndmask_b32_dpp v169, v173, v177, vcc quad_perm:[2,3,0,1] row_mask:0xf bank_mask:0xf
	s_mov_b32 vcc_lo, 0x33333333
	s_mov_b32 vcc_hi, 0x33333333
	s_nop 1
	v_cndmask_b32_dpp v154, v162, v154, vcc quad_perm:[2,3,0,1] row_mask:0xf bank_mask:0xf
	v_cndmask_b32_dpp v170, v174, v170, vcc quad_perm:[2,3,0,1] row_mask:0xf bank_mask:0xf
	v_cndmask_b32_dpp v155, v163, v155, vcc quad_perm:[2,3,0,1] row_mask:0xf bank_mask:0xf
	v_cndmask_b32_dpp v171, v175, v171, vcc quad_perm:[2,3,0,1] row_mask:0xf bank_mask:0xf
	v_cndmask_b32_dpp v156, v164, v156, vcc quad_perm:[2,3,0,1] row_mask:0xf bank_mask:0xf
	v_cndmask_b32_dpp v172, v176, v172, vcc quad_perm:[2,3,0,1] row_mask:0xf bank_mask:0xf
	v_cndmask_b32_dpp v157, v165, v157, vcc quad_perm:[2,3,0,1] row_mask:0xf bank_mask:0xf
	v_cndmask_b32_dpp v173, v177, v173, vcc quad_perm:[2,3,0,1] row_mask:0xf bank_mask:0xf
	global_store_dwordx4 v179, v[154:157], s[82:83] nt
	global_store_dwordx4 v180, v[170:173], s[82:83] nt
	global_store_dwordx4 v181, v[158:161], s[82:83] nt
	global_store_dwordx4 v190, v[166:169], s[82:83] nt
	v_readlane_b32 s2, v239, 0
	s_lshr_b32 s2, s2, 6
	s_add_i32 s2, s2, 6
	s_cmp_gt_u32 s2, 13
	s_cbranch_scc1 .Lhw_seam1_done
	s_add_i32 s2, s2, 14
	s_mul_i32 s2, s2, s74
	v_readlane_b32 s9, v239, 23
	s_lshr_b32 s9, s9, 3
	s_add_i32 s2, s2, s9
	s_cmp_gt_u32 s2, 24575
	s_cbranch_scc1 .Lhw_seam1_done
	v_mbcnt_lo_u32_b32 v178, -1, 0
	v_mbcnt_hi_u32_b32 v178, -1, v178
	v_and_b32_e32 v179, 60, v178
	v_lshlrev_b32_e32 v179, 10, v179
	v_and_b32_e32 v180, 3, v178
	v_lshl_or_b32 v179, v180, 4, v179
	v_add_u32_e32 v180, 0x400, v179
	v_add_u32_e32 v181, 0x800, v179
	v_add_u32_e32 v190, 0xc00, v179
	v_lshlrev_b32_e32 v178, 2, v178
	s_cmp_lt_u32 s2, 16384
	s_cbranch_scc0 .Lhw_dn_s1_1
	s_lshr_b32 s9, s2, 9
	s_bfe_u32 s32, s2, 0x40005
	s_and_b32 s53, s2, 31
	s_lshl_b32 s69, s9, 23
	s_lshl_b32 s100, s32, 19
	s_add_i32 s69, s69, s100
	s_lshl_b32 s100, s53, 8
	s_add_i32 s69, s69, s100
	s_lshl_b32 s98, s9, 11
	s_bfe_u32 s100, s53, 0x30001
	s_lshl_b32 s100, s100, 8
	s_add_i32 s98, s98, s100
	s_lshr_b32 s100, s53, 4
	s_lshl_b32 s100, s100, 7
	s_add_i32 s98, s98, s100
	s_and_b32 s100, s53, 1
	s_lshl_b32 s100, s100, 6
	s_add_i32 s98, s98, s100
	s_lshl_b32 s98, s98, 10
	s_lshl_b32 s100, s32, 6
	s_add_i32 s98, s98, s100
	s_add_i32 s98, s98, 0x2000000
	v_readlane_b32 s82, v239, 11
	v_readlane_b32 s83, v239, 12
	s_movk_i32 s89, 8192
	s_branch .Lhw_go_s1_1

.Lhw_seam2:
	s_mov_b64 exec, -1
	v_readlane_b32 s2, v239, 0
	s_lshr_b32 s2, s2, 6
	s_add_i32 s2, s2, -1
	s_cmp_gt_u32 s2, 13
	s_cbranch_scc1 .Lhw_seam2_done
	s_add_i32 s2, s2, 28
	s_mul_i32 s2, s2, s74
	v_readlane_b32 s9, v239, 23
	s_lshr_b32 s9, s9, 3
	s_add_i32 s2, s2, s9
	s_cmp_gt_u32 s2, 24575
	s_cbranch_scc1 .Lhw_seam2_done
	v_mbcnt_lo_u32_b32 v178, -1, 0
	v_mbcnt_hi_u32_b32 v178, -1, v178
	v_and_b32_e32 v179, 60, v178
	v_lshlrev_b32_e32 v179, 10, v179
	v_and_b32_e32 v180, 3, v178
	v_lshl_or_b32 v179, v180, 4, v179
	v_add_u32_e32 v180, 0x400, v179
	v_add_u32_e32 v181, 0x800, v179
	v_add_u32_e32 v190, 0xc00, v179
	v_lshlrev_b32_e32 v178, 2, v178
	s_cmp_lt_u32 s2, 16384
	s_cbranch_scc0 .Lhw_dn_s2_0
	s_lshr_b32 s9, s2, 9
	s_bfe_u32 s32, s2, 0x40005
	s_and_b32 s53, s2, 31
	s_lshl_b32 s69, s9, 23
	s_lshl_b32 s100, s32, 19
	s_add_i32 s69, s69, s100
	s_lshl_b32 s100, s53, 8
	s_add_i32 s69, s69, s100
	s_lshl_b32 s98, s9, 11
	s_bfe_u32 s100, s53, 0x30001
	s_lshl_b32 s100, s100, 8
	s_add_i32 s98, s98, s100
	s_lshr_b32 s100, s53, 4
	s_lshl_b32 s100, s100, 7
	s_add_i32 s98, s98, s100
	s_and_b32 s100, s53, 1
	s_lshl_b32 s100, s100, 6
	s_add_i32 s98, s98, s100
	s_lshl_b32 s98, s98, 10
	s_lshl_b32 s100, s32, 6
	s_add_i32 s98, s98, s100
	s_add_i32 s98, s98, 0x2000000
	v_readlane_b32 s82, v239, 11
	v_readlane_b32 s83, v239, 12
	s_movk_i32 s89, 8192
	s_branch .Lhw_go_s2_0

.Lhw_go_s2_0:
	s_add_u32 s100, s82, s69
	s_addc_u32 s101, s83, 0
	v_readlane_b32 s82, v239, 44
	v_readlane_b32 s83, v239, 45
	s_add_u32 s82, s82, s98
	s_addc_u32 s83, s83, 0
	global_load_dword v34, v178, s[100:101] nt
	s_add_u32 s100, s100, s89
	s_addc_u32 s101, s101, 0
	global_load_dword v35, v178, s[100:101] nt
	s_add_u32 s100, s100, s89
	s_addc_u32 s101, s101, 0
	global_load_dword v36, v178, s[100:101] nt
	s_add_u32 s100, s100, s89
	s_addc_u32 s101, s101, 0
	global_load_dword v37, v178, s[100:101] nt
	s_add_u32 s100, s100, s89
	s_addc_u32 s101, s101, 0
	global_load_dword v38, v178, s[100:101] nt
	s_add_u32 s100, s100, s89
	s_addc_u32 s101, s101, 0
	global_load_dword v39, v178, s[100:101] nt
	s_add_u32 s100, s100, s89
	s_addc_u32 s101, s101, 0
	global_load_dword v40, v178, s[100:101] nt
	s_add_u32 s100, s100, s89
	s_addc_u32 s101, s101, 0
	global_load_dword v41, v178, s[100:101] nt
	s_add_u32 s100, s100, s89
	s_addc_u32 s101, s101, 0
	global_load_dword v42, v178, s[100:101] nt
	s_add_u32 s100, s100, s89
	s_addc_u32 s101, s101, 0
	global_load_dword v43, v178, s[100:101] nt
	s_add_u32 s100, s100, s89
	s_addc_u32 s101, s101, 0
	global_load_dword v44, v178, s[100:101] nt
	s_add_u32 s100, s100, s89
	s_addc_u32 s101, s101, 0
	global_load_dword v45, v178, s[100:101] nt
	s_add_u32 s100, s100, s89
	s_addc_u32 s101, s101, 0
	global_load_dword v46, v178, s[100:101] nt
	s_add_u32 s100, s100, s89
	s_addc_u32 s101, s101, 0
	global_load_dword v47, v178, s[100:101] nt
	s_add_u32 s100, s100, s89
	s_addc_u32 s101, s101, 0
	global_load_dword v48, v178, s[100:101] nt
	s_add_u32 s100, s100, s89
	s_addc_u32 s101, s101, 0
	global_load_dword v49, v178, s[100:101] nt
	s_add_u32 s100, s100, s89
	s_addc_u32 s101, s101, 0
	global_load_dword v50, v178, s[100:101] nt
	s_add_u32 s100, s100, s89
	s_addc_u32 s101, s101, 0
	global_load_dword v51, v178, s[100:101] nt
	s_add_u32 s100, s100, s89
	s_addc_u32 s101, s101, 0
	global_load_dword v52, v178, s[100:101] nt
	s_add_u32 s100, s100, s89
	s_addc_u32 s101, s101, 0
	global_load_dword v53, v178, s[100:101] nt
	s_add_u32 s100, s100, s89
	s_addc_u32 s101, s101, 0
	global_load_dword v54, v178, s[100:101] nt
	s_add_u32 s100, s100, s89
	s_addc_u32 s101, s101, 0
	global_load_dword v55, v178, s[100:101] nt
	s_add_u32 s100, s100, s89
	s_addc_u32 s101, s101, 0
	global_load_dword v56, v178, s[100:101] nt
	s_add_u32 s100, s100, s89
	s_addc_u32 s101, s101, 0
	global_load_dword v57, v178, s[100:101] nt
	s_add_u32 s100, s100, s89
	s_addc_u32 s101, s101, 0
	global_load_dword v58, v178, s[100:101] nt
	s_add_u32 s100, s100, s89
	s_addc_u32 s101, s101, 0
	global_load_dword v59, v178, s[100:101] nt
	s_add_u32 s100, s100, s89
	s_addc_u32 s101, s101, 0
	global_load_dword v60, v178, s[100:101] nt
	s_add_u32 s100, s100, s89
	s_addc_u32 s101, s101, 0
	global_load_dword v61, v178, s[100:101] nt
	s_add_u32 s100, s100, s89
	s_addc_u32 s101, s101, 0
	global_load_dword v62, v178, s[100:101] nt
	s_add_u32 s100, s100, s89
	s_addc_u32 s101, s101, 0
	global_load_dword v63, v178, s[100:101] nt
	s_add_u32 s100, s100, s89
	s_addc_u32 s101, s101, 0
	global_load_dword v64, v178, s[100:101] nt
	s_add_u32 s100, s100, s89
	s_addc_u32 s101, s101, 0
	global_load_dword v65, v178, s[100:101] nt
	s_add_u32 s100, s100, s89
	s_addc_u32 s101, s101, 0
	global_load_dword v66, v178, s[100:101] nt
	s_add_u32 s100, s100, s89
	s_addc_u32 s101, s101, 0
	global_load_dword v67, v178, s[100:101] nt
	s_add_u32 s100, s100, s89
	s_addc_u32 s101, s101, 0
	global_load_dword v68, v178, s[100:101] nt
	s_add_u32 s100, s100, s89
	s_addc_u32 s101, s101, 0
	global_load_dword v69, v178, s[100:101] nt
	s_add_u32 s100, s100, s89
	s_addc_u32 s101, s101, 0
	global_load_dword v70, v178, s[100:101] nt
	s_add_u32 s100, s100, s89
	s_addc_u32 s101, s101, 0
	global_load_dword v71, v178, s[100:101] nt
	s_add_u32 s100, s100, s89
	s_addc_u32 s101, s101, 0
	global_load_dword v72, v178, s[100:101] nt
	s_add_u32 s100, s100, s89
	s_addc_u32 s101, s101, 0
	global_load_dword v73, v178, s[100:101] nt
	s_add_u32 s100, s100, s89
	s_addc_u32 s101, s101, 0
	global_load_dword v74, v178, s[100:101] nt
	s_add_u32 s100, s100, s89
	s_addc_u32 s101, s101, 0
	global_load_dword v75, v178, s[100:101] nt
	s_add_u32 s100, s100, s89
	s_addc_u32 s101, s101, 0
	global_load_dword v76, v178, s[100:101] nt
	s_add_u32 s100, s100, s89
	s_addc_u32 s101, s101, 0
	global_load_dword v77, v178, s[100:101] nt
	s_add_u32 s100, s100, s89
	s_addc_u32 s101, s101, 0
	global_load_dword v78, v178, s[100:101] nt
	s_add_u32 s100, s100, s89
	s_addc_u32 s101, s101, 0
	global_load_dword v79, v178, s[100:101] nt
	s_add_u32 s100, s100, s89
	s_addc_u32 s101, s101, 0
	global_load_dword v80, v178, s[100:101] nt
	s_add_u32 s100, s100, s89
	s_addc_u32 s101, s101, 0
	global_load_dword v81, v178, s[100:101] nt
	s_add_u32 s100, s100, s89
	s_addc_u32 s101, s101, 0
	global_load_dword v82, v178, s[100:101] nt
	s_add_u32 s100, s100, s89
	s_addc_u32 s101, s101, 0
	global_load_dword v83, v178, s[100:101] nt
	s_add_u32 s100, s100, s89
	s_addc_u32 s101, s101, 0
	global_load_dword v84, v178, s[100:101] nt
	s_add_u32 s100, s100, s89
	s_addc_u32 s101, s101, 0
	global_load_dword v85, v178, s[100:101] nt
	s_add_u32 s100, s100, s89
	s_addc_u32 s101, s101, 0
	global_load_dword v86, v178, s[100:101] nt
	s_add_u32 s100, s100, s89
	s_addc_u32 s101, s101, 0
	global_load_dword v87, v178, s[100:101] nt
	s_add_u32 s100, s100, s89
	s_addc_u32 s101, s101, 0
	global_load_dword v88, v178, s[100:101] nt
	s_add_u32 s100, s100, s89
	s_addc_u32 s101, s101, 0
	global_load_dword v89, v178, s[100:101] nt
	s_add_u32 s100, s100, s89
	s_addc_u32 s101, s101, 0
	global_load_dword v90, v178, s[100:101] nt
	s_add_u32 s100, s100, s89
	s_addc_u32 s101, s101, 0
	global_load_dword v91, v178, s[100:101] nt
	s_add_u32 s100, s100, s89
	s_addc_u32 s101, s101, 0
	global_load_dword v92, v178, s[100:101] nt
	s_add_u32 s100, s100, s89
	s_addc_u32 s101, s101, 0
	global_load_dword v93, v178, s[100:101] nt
	s_add_u32 s100, s100, s89
	s_addc_u32 s101, s101, 0
	global_load_dword v94, v178, s[100:101] nt
	s_add_u32 s100, s100, s89
	s_addc_u32 s101, s101, 0
	global_load_dword v95, v178, s[100:101] nt
	s_add_u32 s100, s100, s89
	s_addc_u32 s101, s101, 0
	global_load_dword v96, v178, s[100:101] nt
	s_add_u32 s100, s100, s89
	s_addc_u32 s101, s101, 0
	global_load_dword v97, v178, s[100:101] nt
	s_add_u32 s100, s100, s89
	s_addc_u32 s101, s101, 0
	s_waitcnt vmcnt(48)
	v_mul_f32_e32 v34, 0x42000000, v34
	v_mul_f32_e32 v35, 0x42000000, v35
	v_mul_f32_e32 v36, 0x42000000, v36
	v_mul_f32_e32 v37, 0x42000000, v37
	v_mul_f32_e32 v38, 0x42000000, v38
	v_mul_f32_e32 v39, 0x42000000, v39
	v_mul_f32_e32 v40, 0x42000000, v40
	v_mul_f32_e32 v41, 0x42000000, v41
	v_mul_f32_e32 v42, 0x42000000, v42
	v_mul_f32_e32 v43, 0x42000000, v43
	v_mul_f32_e32 v44, 0x42000000, v44
	v_mul_f32_e32 v45, 0x42000000, v45
	v_mul_f32_e32 v46, 0x42000000, v46
	v_mul_f32_e32 v47, 0x42000000, v47
	v_mul_f32_e32 v48, 0x42000000, v48
	v_mul_f32_e32 v49, 0x42000000, v49
	v_cvt_pk_fp8_f32 v154, v34, v35
	v_cvt_pk_fp8_f32 v155, v38, v39
	v_cvt_pk_fp8_f32 v156, v42, v43
	v_cvt_pk_fp8_f32 v157, v46, v47
	v_cvt_pk_fp8_f32 v154, v36, v37 op_sel:[0,0,1]
	v_cvt_pk_fp8_f32 v155, v40, v41 op_sel:[0,0,1]
	v_cvt_pk_fp8_f32 v156, v44, v45 op_sel:[0,0,1]
	v_cvt_pk_fp8_f32 v157, v48, v49 op_sel:[0,0,1]
	s_waitcnt vmcnt(32)
	v_mul_f32_e32 v50, 0x42000000, v50
	v_mul_f32_e32 v51, 0x42000000, v51
	v_mul_f32_e32 v52, 0x42000000, v52
	v_mul_f32_e32 v53, 0x42000000, v53
	v_mul_f32_e32 v54, 0x42000000, v54
	v_mul_f32_e32 v55, 0x42000000, v55
	v_mul_f32_e32 v56, 0x42000000, v56
	v_mul_f32_e32 v57, 0x42000000, v57
	v_mul_f32_e32 v58, 0x42000000, v58
	v_mul_f32_e32 v59, 0x42000000, v59
	v_mul_f32_e32 v60, 0x42000000, v60
	v_mul_f32_e32 v61, 0x42000000, v61
	v_mul_f32_e32 v62, 0x42000000, v62
	v_mul_f32_e32 v63, 0x42000000, v63
	v_mul_f32_e32 v64, 0x42000000, v64
	v_mul_f32_e32 v65, 0x42000000, v65
	v_cvt_pk_fp8_f32 v158, v50, v51
	v_cvt_pk_fp8_f32 v159, v54, v55
	v_cvt_pk_fp8_f32 v160, v58, v59
	v_cvt_pk_fp8_f32 v161, v62, v63
	v_cvt_pk_fp8_f32 v158, v52, v53 op_sel:[0,0,1]
	v_cvt_pk_fp8_f32 v159, v56, v57 op_sel:[0,0,1]
	v_cvt_pk_fp8_f32 v160, v60, v61 op_sel:[0,0,1]
	v_cvt_pk_fp8_f32 v161, v64, v65 op_sel:[0,0,1]
	s_waitcnt vmcnt(16)
	v_mul_f32_e32 v66, 0x42000000, v66
	v_mul_f32_e32 v67, 0x42000000, v67
	v_mul_f32_e32 v68, 0x42000000, v68
	v_mul_f32_e32 v69, 0x42000000, v69
	v_mul_f32_e32 v70, 0x42000000, v70
	v_mul_f32_e32 v71, 0x42000000, v71
	v_mul_f32_e32 v72, 0x42000000, v72
	v_mul_f32_e32 v73, 0x42000000, v73
	v_mul_f32_e32 v74, 0x42000000, v74
	v_mul_f32_e32 v75, 0x42000000, v75
	v_mul_f32_e32 v76, 0x42000000, v76
	v_mul_f32_e32 v77, 0x42000000, v77
	v_mul_f32_e32 v78, 0x42000000, v78
	v_mul_f32_e32 v79, 0x42000000, v79
	v_mul_f32_e32 v80, 0x42000000, v80
	v_mul_f32_e32 v81, 0x42000000, v81
	v_cvt_pk_fp8_f32 v162, v66, v67
	v_cvt_pk_fp8_f32 v163, v70, v71
	v_cvt_pk_fp8_f32 v164, v74, v75
	v_cvt_pk_fp8_f32 v165, v78, v79
	v_cvt_pk_fp8_f32 v162, v68, v69 op_sel:[0,0,1]
	v_cvt_pk_fp8_f32 v163, v72, v73 op_sel:[0,0,1]
	v_cvt_pk_fp8_f32 v164, v76, v77 op_sel:[0,0,1]
	v_cvt_pk_fp8_f32 v165, v80, v81 op_sel:[0,0,1]
	s_waitcnt vmcnt(0)
	v_mul_f32_e32 v82, 0x42000000, v82
	v_mul_f32_e32 v83, 0x42000000, v83
	v_mul_f32_e32 v84, 0x42000000, v84
	v_mul_f32_e32 v85, 0x42000000, v85
	v_mul_f32_e32 v86, 0x42000000, v86
	v_mul_f32_e32 v87, 0x42000000, v87
	v_mul_f32_e32 v88, 0x42000000, v88
	v_mul_f32_e32 v89, 0x42000000, v89
	v_mul_f32_e32 v90, 0x42000000, v90
	v_mul_f32_e32 v91, 0x42000000, v91
	v_mul_f32_e32 v92, 0x42000000, v92
	v_mul_f32_e32 v93, 0x42000000, v93
	v_mul_f32_e32 v94, 0x42000000, v94
	v_mul_f32_e32 v95, 0x42000000, v95
	v_mul_f32_e32 v96, 0x42000000, v96
	v_mul_f32_e32 v97, 0x42000000, v97
	v_cvt_pk_fp8_f32 v166, v82, v83
	v_cvt_pk_fp8_f32 v167, v86, v87
	v_cvt_pk_fp8_f32 v168, v90, v91
	v_cvt_pk_fp8_f32 v169, v94, v95
	v_cvt_pk_fp8_f32 v166, v84, v85 op_sel:[0,0,1]
	v_cvt_pk_fp8_f32 v167, v88, v89 op_sel:[0,0,1]
	v_cvt_pk_fp8_f32 v168, v92, v93 op_sel:[0,0,1]
	v_cvt_pk_fp8_f32 v169, v96, v97 op_sel:[0,0,1]
	s_mov_b32 vcc_lo, 0xaaaaaaaa
	s_mov_b32 vcc_hi, 0xaaaaaaaa
	s_nop 1
	v_cndmask_b32_dpp v170, v154, v158, vcc quad_perm:[1,0,3,2] row_mask:0xf bank_mask:0xf
	v_cndmask_b32_dpp v174, v162, v166, vcc quad_perm:[1,0,3,2] row_mask:0xf bank_mask:0xf
	v_cndmask_b32_dpp v171, v155, v159, vcc quad_perm:[1,0,3,2] row_mask:0xf bank_mask:0xf
	v_cndmask_b32_dpp v175, v163, v167, vcc quad_perm:[1,0,3,2] row_mask:0xf bank_mask:0xf
	v_cndmask_b32_dpp v172, v156, v160, vcc quad_perm:[1,0,3,2] row_mask:0xf bank_mask:0xf
	v_cndmask_b32_dpp v176, v164, v168, vcc quad_perm:[1,0,3,2] row_mask:0xf bank_mask:0xf
	v_cndmask_b32_dpp v173, v157, v161, vcc quad_perm:[1,0,3,2] row_mask:0xf bank_mask:0xf
	v_cndmask_b32_dpp v177, v165, v169, vcc quad_perm:[1,0,3,2] row_mask:0xf bank_mask:0xf
	s_mov_b32 vcc_lo, 0x55555555
	s_mov_b32 vcc_hi, 0x55555555
	s_nop 1
	v_cndmask_b32_dpp v154, v158, v154, vcc quad_perm:[1,0,3,2] row_mask:0xf bank_mask:0xf
	v_cndmask_b32_dpp v162, v166, v162, vcc quad_perm:[1,0,3,2] row_mask:0xf bank_mask:0xf
	v_cndmask_b32_dpp v155, v159, v155, vcc quad_perm:[1,0,3,2] row_mask:0xf bank_mask:0xf
	v_cndmask_b32_dpp v163, v167, v163, vcc quad_perm:[1,0,3,2] row_mask:0xf bank_mask:0xf
	v_cndmask_b32_dpp v156, v160, v156, vcc quad_perm:[1,0,3,2] row_mask:0xf bank_mask:0xf
	v_cndmask_b32_dpp v164, v168, v164, vcc quad_perm:[1,0,3,2] row_mask:0xf bank_mask:0xf
	v_cndmask_b32_dpp v157, v161, v157, vcc quad_perm:[1,0,3,2] row_mask:0xf bank_mask:0xf
	v_cndmask_b32_dpp v165, v169, v165, vcc quad_perm:[1,0,3,2] row_mask:0xf bank_mask:0xf
	s_mov_b32 vcc_lo, 0xcccccccc
	s_mov_b32 vcc_hi, 0xcccccccc
	s_nop 1
	v_cndmask_b32_dpp v158, v154, v162, vcc quad_perm:[2,3,0,1] row_mask:0xf bank_mask:0xf
	v_cndmask_b32_dpp v166, v170, v174, vcc quad_perm:[2,3,0,1] row_mask:0xf bank_mask:0xf
	v_cndmask_b32_dpp v159, v155, v163, vcc quad_perm:[2,3,0,1] row_mask:0xf bank_mask:0xf
	v_cndmask_b32_dpp v167, v171, v175, vcc quad_perm:[2,3,0,1] row_mask:0xf bank_mask:0xf
	v_cndmask_b32_dpp v160, v156, v164, vcc quad_perm:[2,3,0,1] row_mask:0xf bank_mask:0xf
	v_cndmask_b32_dpp v168, v172, v176, vcc quad_perm:[2,3,0,1] row_mask:0xf bank_mask:0xf
	v_cndmask_b32_dpp v161, v157, v165, vcc quad_perm:[2,3,0,1] row_mask:0xf bank_mask:0xf
	v_cndmask_b32_dpp v169, v173, v177, vcc quad_perm:[2,3,0,1] row_mask:0xf bank_mask:0xf
	s_mov_b32 vcc_lo, 0x33333333
	s_mov_b32 vcc_hi, 0x33333333
	s_nop 1
	v_cndmask_b32_dpp v154, v162, v154, vcc quad_perm:[2,3,0,1] row_mask:0xf bank_mask:0xf
	v_cndmask_b32_dpp v170, v174, v170, vcc quad_perm:[2,3,0,1] row_mask:0xf bank_mask:0xf
	v_cndmask_b32_dpp v155, v163, v155, vcc quad_perm:[2,3,0,1] row_mask:0xf bank_mask:0xf
	v_cndmask_b32_dpp v171, v175, v171, vcc quad_perm:[2,3,0,1] row_mask:0xf bank_mask:0xf
	v_cndmask_b32_dpp v156, v164, v156, vcc quad_perm:[2,3,0,1] row_mask:0xf bank_mask:0xf
	v_cndmask_b32_dpp v172, v176, v172, vcc quad_perm:[2,3,0,1] row_mask:0xf bank_mask:0xf
	v_cndmask_b32_dpp v157, v165, v157, vcc quad_perm:[2,3,0,1] row_mask:0xf bank_mask:0xf
	v_cndmask_b32_dpp v173, v177, v173, vcc quad_perm:[2,3,0,1] row_mask:0xf bank_mask:0xf
	global_store_dwordx4 v179, v[154:157], s[82:83] nt
	global_store_dwordx4 v180, v[170:173], s[82:83] nt
	global_store_dwordx4 v181, v[158:161], s[82:83] nt
	global_store_dwordx4 v190, v[166:169], s[82:83] nt
	v_readlane_b32 s2, v239, 0
	s_lshr_b32 s2, s2, 6
	s_add_i32 s2, s2, 6
	s_cmp_gt_u32 s2, 13
	s_cbranch_scc1 .Lhw_seam2_done
	s_add_i32 s2, s2, 28
	s_mul_i32 s2, s2, s74
	v_readlane_b32 s9, v239, 23
	s_lshr_b32 s9, s9, 3
	s_add_i32 s2, s2, s9
	s_cmp_gt_u32 s2, 24575
	s_cbranch_scc1 .Lhw_seam2_done
	v_mbcnt_lo_u32_b32 v178, -1, 0
	v_mbcnt_hi_u32_b32 v178, -1, v178
	v_and_b32_e32 v179, 60, v178
	v_lshlrev_b32_e32 v179, 10, v179
	v_and_b32_e32 v180, 3, v178
	v_lshl_or_b32 v179, v180, 4, v179
	v_add_u32_e32 v180, 0x400, v179
	v_add_u32_e32 v181, 0x800, v179
	v_add_u32_e32 v190, 0xc00, v179
	v_lshlrev_b32_e32 v178, 2, v178
	s_cmp_lt_u32 s2, 16384
	s_cbranch_scc0 .Lhw_dn_s2_1
	s_lshr_b32 s9, s2, 9
	s_bfe_u32 s32, s2, 0x40005
	s_and_b32 s53, s2, 31
	s_lshl_b32 s69, s9, 23
	s_lshl_b32 s100, s32, 19
	s_add_i32 s69, s69, s100
	s_lshl_b32 s100, s53, 8
	s_add_i32 s69, s69, s100
	s_lshl_b32 s98, s9, 11
	s_bfe_u32 s100, s53, 0x30001
	s_lshl_b32 s100, s100, 8
	s_add_i32 s98, s98, s100
	s_lshr_b32 s100, s53, 4
	s_lshl_b32 s100, s100, 7
	s_add_i32 s98, s98, s100
	s_and_b32 s100, s53, 1
	s_lshl_b32 s100, s100, 6
	s_add_i32 s98, s98, s100
	s_lshl_b32 s98, s98, 10
	s_lshl_b32 s100, s32, 6
	s_add_i32 s98, s98, s100
	s_add_i32 s98, s98, 0x2000000
	v_readlane_b32 s82, v239, 11
	v_readlane_b32 s83, v239, 12
	s_movk_i32 s89, 8192
	s_branch .Lhw_go_s2_1
